# speedup vs baseline: 1.0166x; 1.0166x over previous
.LBB0_2:
	s_or_b64 exec, exec, s[10:11]
	s_load_dwordx2 s[8:9], s[0:1], 0x10
	v_and_b32_e32 v34, 63, v0
	v_lshrrev_b32_e32 v39, 6, v0
	v_mov_b32_e32 v38, 0x3c0
	v_cmp_eq_u32_e64 s[6:7], 0, v34
	v_mad_u32_u24 v38, v39, 48, v38
	v_add_f32_dpp v145, v145, v145 row_ror:8 row_mask:0xf bank_mask:0xf bound_ctrl:1
	v_add_f32_dpp v143, v143, v143 row_ror:8 row_mask:0xf bank_mask:0xf bound_ctrl:1
	v_add_f32_dpp v144, v144, v144 row_ror:8 row_mask:0xf bank_mask:0xf bound_ctrl:1
	v_add_f32_dpp v142, v142, v142 row_ror:8 row_mask:0xf bank_mask:0xf bound_ctrl:1
	v_add_f32_dpp v141, v141, v141 row_ror:8 row_mask:0xf bank_mask:0xf bound_ctrl:1
	v_add_f32_dpp v139, v139, v139 row_ror:8 row_mask:0xf bank_mask:0xf bound_ctrl:1
	v_add_f32_dpp v140, v140, v140 row_ror:8 row_mask:0xf bank_mask:0xf bound_ctrl:1
	v_add_f32_dpp v138, v138, v138 row_ror:8 row_mask:0xf bank_mask:0xf bound_ctrl:1
	v_add_f32_dpp v137, v137, v137 row_ror:8 row_mask:0xf bank_mask:0xf bound_ctrl:1
	v_add_f32_dpp v72, v72, v72 row_ror:8 row_mask:0xf bank_mask:0xf bound_ctrl:1
	v_add_f32_dpp v73, v73, v73 row_ror:8 row_mask:0xf bank_mask:0xf bound_ctrl:1
	v_add_f32_dpp v71, v71, v71 row_ror:8 row_mask:0xf bank_mask:0xf bound_ctrl:1
	v_add_f32_dpp v145, v145, v145 row_ror:4 row_mask:0xf bank_mask:0xf bound_ctrl:1
	v_add_f32_dpp v143, v143, v143 row_ror:4 row_mask:0xf bank_mask:0xf bound_ctrl:1
	v_add_f32_dpp v144, v144, v144 row_ror:4 row_mask:0xf bank_mask:0xf bound_ctrl:1
	v_add_f32_dpp v142, v142, v142 row_ror:4 row_mask:0xf bank_mask:0xf bound_ctrl:1
	v_add_f32_dpp v141, v141, v141 row_ror:4 row_mask:0xf bank_mask:0xf bound_ctrl:1
	v_add_f32_dpp v139, v139, v139 row_ror:4 row_mask:0xf bank_mask:0xf bound_ctrl:1
	v_add_f32_dpp v140, v140, v140 row_ror:4 row_mask:0xf bank_mask:0xf bound_ctrl:1
	v_add_f32_dpp v138, v138, v138 row_ror:4 row_mask:0xf bank_mask:0xf bound_ctrl:1
	v_add_f32_dpp v137, v137, v137 row_ror:4 row_mask:0xf bank_mask:0xf bound_ctrl:1
	v_add_f32_dpp v72, v72, v72 row_ror:4 row_mask:0xf bank_mask:0xf bound_ctrl:1
	v_add_f32_dpp v73, v73, v73 row_ror:4 row_mask:0xf bank_mask:0xf bound_ctrl:1
	v_add_f32_dpp v71, v71, v71 row_ror:4 row_mask:0xf bank_mask:0xf bound_ctrl:1
	v_add_f32_dpp v145, v145, v145 row_ror:2 row_mask:0xf bank_mask:0xf bound_ctrl:1
	v_add_f32_dpp v143, v143, v143 row_ror:2 row_mask:0xf bank_mask:0xf bound_ctrl:1
	v_add_f32_dpp v144, v144, v144 row_ror:2 row_mask:0xf bank_mask:0xf bound_ctrl:1
	v_add_f32_dpp v142, v142, v142 row_ror:2 row_mask:0xf bank_mask:0xf bound_ctrl:1
	v_add_f32_dpp v141, v141, v141 row_ror:2 row_mask:0xf bank_mask:0xf bound_ctrl:1
	v_add_f32_dpp v139, v139, v139 row_ror:2 row_mask:0xf bank_mask:0xf bound_ctrl:1
	v_add_f32_dpp v140, v140, v140 row_ror:2 row_mask:0xf bank_mask:0xf bound_ctrl:1
	v_add_f32_dpp v138, v138, v138 row_ror:2 row_mask:0xf bank_mask:0xf bound_ctrl:1
	v_add_f32_dpp v137, v137, v137 row_ror:2 row_mask:0xf bank_mask:0xf bound_ctrl:1
	v_add_f32_dpp v72, v72, v72 row_ror:2 row_mask:0xf bank_mask:0xf bound_ctrl:1
	v_add_f32_dpp v73, v73, v73 row_ror:2 row_mask:0xf bank_mask:0xf bound_ctrl:1
	v_add_f32_dpp v71, v71, v71 row_ror:2 row_mask:0xf bank_mask:0xf bound_ctrl:1
	v_add_f32_dpp v145, v145, v145 row_ror:1 row_mask:0xf bank_mask:0xf bound_ctrl:1
	v_add_f32_dpp v143, v143, v143 row_ror:1 row_mask:0xf bank_mask:0xf bound_ctrl:1
	v_add_f32_dpp v144, v144, v144 row_ror:1 row_mask:0xf bank_mask:0xf bound_ctrl:1
	v_add_f32_dpp v142, v142, v142 row_ror:1 row_mask:0xf bank_mask:0xf bound_ctrl:1
	v_add_f32_dpp v141, v141, v141 row_ror:1 row_mask:0xf bank_mask:0xf bound_ctrl:1
	v_add_f32_dpp v139, v139, v139 row_ror:1 row_mask:0xf bank_mask:0xf bound_ctrl:1
	v_add_f32_dpp v140, v140, v140 row_ror:1 row_mask:0xf bank_mask:0xf bound_ctrl:1
	v_add_f32_dpp v138, v138, v138 row_ror:1 row_mask:0xf bank_mask:0xf bound_ctrl:1
	v_add_f32_dpp v137, v137, v137 row_ror:1 row_mask:0xf bank_mask:0xf bound_ctrl:1
	v_add_f32_dpp v72, v72, v72 row_ror:1 row_mask:0xf bank_mask:0xf bound_ctrl:1
	v_add_f32_dpp v73, v73, v73 row_ror:1 row_mask:0xf bank_mask:0xf bound_ctrl:1
	v_add_f32_dpp v71, v71, v71 row_ror:1 row_mask:0xf bank_mask:0xf bound_ctrl:1
	v_add_f32_dpp v145, v145, v145 row_bcast:15 row_mask:0xa bank_mask:0xf
	v_add_f32_dpp v143, v143, v143 row_bcast:15 row_mask:0xa bank_mask:0xf
	v_add_f32_dpp v144, v144, v144 row_bcast:15 row_mask:0xa bank_mask:0xf
	v_add_f32_dpp v142, v142, v142 row_bcast:15 row_mask:0xa bank_mask:0xf
	v_add_f32_dpp v141, v141, v141 row_bcast:15 row_mask:0xa bank_mask:0xf
	v_add_f32_dpp v139, v139, v139 row_bcast:15 row_mask:0xa bank_mask:0xf
	v_add_f32_dpp v140, v140, v140 row_bcast:15 row_mask:0xa bank_mask:0xf
	v_add_f32_dpp v138, v138, v138 row_bcast:15 row_mask:0xa bank_mask:0xf
	v_add_f32_dpp v137, v137, v137 row_bcast:15 row_mask:0xa bank_mask:0xf
	v_add_f32_dpp v72, v72, v72 row_bcast:15 row_mask:0xa bank_mask:0xf
	v_add_f32_dpp v73, v73, v73 row_bcast:15 row_mask:0xa bank_mask:0xf
	v_add_f32_dpp v71, v71, v71 row_bcast:15 row_mask:0xa bank_mask:0xf
	v_add_f32_dpp v152, v145, v145 row_bcast:31 row_mask:0xc bank_mask:0xf
	v_add_f32_dpp v153, v143, v143 row_bcast:31 row_mask:0xc bank_mask:0xf
	v_add_f32_dpp v154, v144, v144 row_bcast:31 row_mask:0xc bank_mask:0xf
	v_add_f32_dpp v155, v142, v142 row_bcast:31 row_mask:0xc bank_mask:0xf
	v_add_f32_dpp v156, v141, v141 row_bcast:31 row_mask:0xc bank_mask:0xf
	v_add_f32_dpp v157, v139, v139 row_bcast:31 row_mask:0xc bank_mask:0xf
	v_add_f32_dpp v158, v140, v140 row_bcast:31 row_mask:0xc bank_mask:0xf
	v_add_f32_dpp v159, v138, v138 row_bcast:31 row_mask:0xc bank_mask:0xf
	v_add_f32_dpp v34, v137, v137 row_bcast:31 row_mask:0xc bank_mask:0xf
	v_add_f32_dpp v35, v72, v72 row_bcast:31 row_mask:0xc bank_mask:0xf
	v_add_f32_dpp v36, v73, v73 row_bcast:31 row_mask:0xc bank_mask:0xf
	v_add_f32_dpp v37, v71, v71 row_bcast:31 row_mask:0xc bank_mask:0xf
	s_mov_b32 exec_lo, 0
	s_mov_b32 exec_hi, 0x80000000
	ds_write_b128 v38, v[152:155]
	ds_write_b128 v38, v[156:159] offset:16
	ds_write_b128 v38, v[34:37] offset:32
	s_mov_b64 exec, -1
	v_cmp_gt_u32_e32 vcc, 12, v0
	v_lshlrev_b32_e32 v34, 2, v0
	s_waitcnt lgkmcnt(0)
	s_barrier
	s_load_dwordx4 s[12:15], s[0:1], 0x20
	s_load_dwordx2 s[10:11], s[0:1], 0x18
	s_mov_b32 s20, 0
	s_mov_b32 s21, 0xc1f00000
	s_mov_b32 s23, 0xffffffe0
	s_and_saveexec_b64 s[16:17], vcc
	s_cbranch_execz .Lkf_pub_done
	ds_read2_b32 v[36:37], v34 offset0:240 offset1:252
	v_add_u32_e32 v35, 0x400, v34
	ds_read2_b32 v[42:43], v35 offset0:8 offset1:20
	ds_read2_b32 v[44:45], v35 offset0:32 offset1:44
	ds_read2_b32 v[48:49], v35 offset0:56 offset1:68
	ds_read2_b32 v[52:53], v35 offset0:80 offset1:92
	ds_read2_b32 v[152:153], v35 offset0:104 offset1:116
	s_mul_i32 s18, s2, 48
	s_mul_hi_i32 s19, s2, 48
	s_waitcnt lgkmcnt(0)
	v_add_f32_e32 v36, 0, v36
	v_add_f32_e32 v36, v36, v37
	v_add_f32_e32 v36, v36, v42
	v_add_f32_e32 v36, v36, v43
	v_add_f32_e32 v36, v36, v44
	v_add_f32_e32 v36, v36, v45
	v_add_f32_e32 v36, v36, v48
	v_add_f32_e32 v36, v36, v49
	v_add_f32_e32 v36, v36, v52
	v_add_f32_e32 v36, v36, v53
	v_add_f32_e32 v36, v36, v152
	s_add_u32 s18, s8, s18
	v_add_f32_e32 v35, v36, v153
	s_addc_u32 s19, s9, s19
	v_and_b32_e32 v38, 3, v0
	v_lshrrev_b32_e32 v41, 2, v0
	global_store_dword v34, v35, s[18:19] nt
	v_cmp_ne_u32_e32 vcc, 3, v38
	s_and_b64 exec, exec, vcc
	s_cbranch_execz .Lkf_pub_done
	v_cmp_eq_u32_e32 vcc, 0, v38
	v_cvt_f64_f32_e32 v[42:43], v35
	s_lshl_b32 s18, s24, 4
	s_add_i32 s18, s18, s3
	v_cndmask_b32_e64 v37, 24, 0, vcc
	v_ldexp_f64 v[42:43], v[42:43], v37
	s_mulk_i32 s18, 0x60
	v_lshlrev_b32_e32 v41, 5, v41
	v_ldexp_f64 v[44:45], v[42:43], s23
	v_lshl_add_u32 v41, v38, 3, v41
	v_floor_f64_e32 v[44:45], v[44:45]
	v_add_u32_e32 v41, s18, v41
	v_fma_f64 v[48:49], v[44:45], s[20:21], v[42:43]
	v_cvt_i32_f64_e32 v37, v[44:45]
	v_cvt_u32_f64_e32 v36, v[48:49]
	s_nop 0
	v_lshlrev_b64 v[36:37], 8, v[36:37]
	s_nop 0
	v_or_b32_e32 v36, 1, v36
	s_nop 0
	global_atomic_add_x2 v41, v[36:37], s[14:15]
